# next-unit prefetch in gate/up: during a unit's epilogue the workgroup walks to its next unit, loads its token list and gathers its first A tile into LDS; the next prologue skips both
# baseline (speedup 1.0000x reference)
; #define G_DMA_A(buf, t, i_) __builtin_amdgcn_raw_ptr_buffer_load_lds(ra, (LAS void*)(lds + (buf) * 65536 + a_wu + (i_) * 8192), 16, ao##i_, (unsigned)(t) * 128u, 0, 0)
; #define G_ISSUE_B(t) do { const unsigned so_ = (unsigned)(t) * 64u * ldbB; _Pragma("unroll") for (int i_ = 0; i_ < 8; ++i_) sb[i_] = __builtin_bit_cast(f32x4, __builtin_amdgcn_raw_buffer_load_b128(rb, bo, so_ + (unsigned)i_ * ldbB, 0)); } while (0)
; #define G_RETIRE() asm volatile("s_waitcnt vmcnt(0)" : "+v"(sb[0]), "+v"(sb[1]), "+v"(sb[2]), "+v"(sb[3]), "+v"(sb[4]), "+v"(sb[5]), "+v"(sb[6]), "+v"(sb[7]) :: "memory")
; #define G_WRITE_B(buf) do { LAS unsigned char* d_ = lds + (buf) * 65536; \
;         _Pragma("unroll") for (int j_ = 0; j_ < 4; ++j_) { u32x4 w_; w_.x = cvtpk(sb[0][j_], sb[1][j_]); w_.y = cvtpk(sb[2][j_], sb[3][j_]); w_.z = cvtpk(sb[4][j_], sb[5][j_]); w_.w = cvtpk(sb[6][j_], sb[7][j_]); \
;             *(LAS u32x4*)(d_ + 32768 + T.b_w + ((T.b_rot + 64u * j_) & 255u)) = w_; } } while (0)
; __device__ __forceinline__ void gemm_kloop_light(f32x4 (&acc)[8][4], LAS unsigned char* lds, const GemmT& T, ...
;     ...
;     G_ISSUE_B(0); G_DMA_A(0, 0, 0); G_DMA_A(0, 0, 1); G_DMA_A(0, 0, 2); G_DMA_A(0, 0, 3); G_RETIRE(); G_WRITE_B(0);
;     if (nt > 1) G_ISSUE_B(1);
; __device__ __forceinline__ void phase_moe_gu(const Ptrs& p, LAS unsigned char* lds) {
;     ...
;         const int* list = (const int*)(p.ws + OFF_LIST) + (size_t)mu.e * NTOK; const int i0 = mu.mt * 256, n0 = mu.nt * 128;
;         unsigned ao[4];
; #pragma unroll
;         for (int i = 0; i < 4; ++i) { const int r = i0 + T.aR + 64 * i; const int tok = (r < mu.cnt) ? (list[r] >> 2) : 0; ao[i] = (unsigned)((tok * D + T.aC) * 2); }
;         const float* wsel = ((__builtin_amdgcn_readfirstlane(T.b_p) & 1) ? p.w_up : p.w_gate) + (size_t)mu.e * D * D + n0;
;         const unsigned bo = (unsigned)((T.b_k * D + T.b_gucol) * 4);
;         f32x4 acc[8][4]; acc_zero(acc);
;         const int mlim = __builtin_amdgcn_readfirstlane(T.wr) ? 0 : ((mu.cnt - i0 + 15) >> 4);
;         if (mu.light) gemm_kloop_light(acc, lds, T, mk_rsrc(h2), ao[0], ao[1], ao[2], ao[3], mk_rsrc(wsel), bo, D * 4u, D / 64, mlim);
;         else gemm_kloop(acc, lds, T, mk_rsrc(h2), ao[0], ao[1], ao[2], ao[3], mk_rsrc(wsel), bo, D * 4u, D / 64);
.LBB0_1163:
	s_andn2_b64 vcc, exec, s[0:1]
	s_mov_b64 s[0:1], -1
	s_cbranch_vccnz .LBB0_1005
	s_ashr_i32 s43, s42, 31
	s_lshl_b64 s[0:1], s[42:43], 15
	v_mov_b32_e32 v3, v0
	s_add_u32 s0, s52, s0
	s_addc_u32 s1, s53, s1
	v_bfe_u32 v4, v3, 2, 4
	s_lshl_b32 s2, s86, 8
	v_ashrrev_i32_e32 v10, 7, v3
	v_or_b32_e32 v4, s2, v4
	v_lshl_add_u32 v4, v10, 4, v4
	s_cmp_lg_u32 s98, 0
	s_cbranch_scc1 .Lmy_pf_use
	v_cmp_gt_i32_e32 vcc, s87, v4
	v_mov_b32_e32 v6, 0
	v_ashrrev_i32_e32 v5, 31, v4
	v_mov_b32_e32 v7, 0
	v_mov_b32_e32 v8, 0
	v_mov_b32_e32 v9, 0
	v_lshl_add_u64 v[12:13], v[4:5], 2, s[0:1]
	s_and_saveexec_b64 s[4:5], vcc
	global_load_dword v7, v[12:13], off
	s_or_b64 exec, exec, s[4:5]
	v_add_u32_e32 v11, 64, v4
	v_cmp_gt_i32_e32 vcc, s87, v11
	s_and_saveexec_b64 s[4:5], vcc
	global_load_dword v6, v[12:13], off offset:256
	s_or_b64 exec, exec, s[4:5]
	v_add_u32_e32 v11, 0x80, v4
	v_cmp_gt_i32_e32 vcc, s87, v11
	s_and_saveexec_b64 s[4:5], vcc
	global_load_dword v9, v[12:13], off offset:512
	s_or_b64 exec, exec, s[4:5]
	v_add_u32_e32 v11, 0xc0, v4
	v_cmp_gt_i32_e32 vcc, s87, v11
	s_and_saveexec_b64 s[4:5], vcc
	global_load_dword v8, v[12:13], off offset:768
	s_or_b64 exec, exec, s[4:5]
	s_branch .Lmy_pf_done
.Lmy_pf_use:
	v_mov_b32_e32 v7, v247
	v_mov_b32_e32 v6, v248
	v_mov_b32_e32 v9, v249
	v_mov_b32_e32 v8, v250
.Lmy_pf_done:
	v_ashrrev_i32_e32 v5, 6, v3
	v_and_b32_e32 v11, 1, v5
	s_lshl_b32 s0, s85, 7
	v_readfirstlane_b32 s1, v11
	v_readlane_b32 s4, v246, 0
	s_bitcmp0_b32 s1, 0
	v_readlane_b32 s5, v246, 1
	s_cselect_b32 s1, s49, s5
	s_cselect_b32 s3, s48, s4
	s_lshl_b64 s[4:5], s[42:43], 24
	v_readlane_b32 s6, v246, 2
	s_add_u32 s3, s3, s4
	v_and_b32_e32 v4, 63, v3
	s_addc_u32 s6, s1, s5
	s_ashr_i32 s1, s0, 31
	v_lshrrev_b32_e32 v12, 5, v4
	v_bfe_u32 v13, v3, 1, 2
	s_lshl_b64 s[4:5], s[0:1], 2
	v_lshl_or_b32 v10, v10, 1, v12
	v_bfe_u32 v12, v3, 3, 2
	v_and_b32_e32 v14, 1, v3
	v_lshlrev_b32_e32 v15, 5, v13
	s_add_u32 s24, s3, s4
	v_lshl_or_b32 v15, v12, 7, v15
	v_lshlrev_b32_e32 v16, 16, v10
	v_lshlrev_b32_e32 v17, 4, v14
	s_addc_u32 s1, s6, s5
	v_or3_b32 v225, v15, v17, v16
	s_and_b32 s25, s1, 0xffff
	s_movk_i32 s1, 0x2000
	buffer_load_dwordx4 v[114:117], v225, s[24:27], 0 offen
	buffer_load_dwordx4 v[118:121], v225, s[24:27], s66 offen
	s_mov_b32 s3, 0x8000
	buffer_load_dwordx4 v[126:129], v225, s[24:27], s1 offen
	buffer_load_dwordx4 v[122:125], v225, s[24:27], s3 offen
	s_movk_i32 s1, 0x4000
	s_mov_b32 s3, 0xa000
	buffer_load_dwordx4 v[130:133], v225, s[24:27], s1 offen
	buffer_load_dwordx4 v[134:137], v225, s[24:27], s3 offen
	s_mov_b32 s1, 0xc000
	s_mov_b32 s3, 0xe000
	buffer_load_dwordx4 v[142:145], v225, s[24:27], s1 offen
	buffer_load_dwordx4 v[146:149], v225, s[24:27], s3 offen
	s_cmp_lg_u32 s98, 0
	s_cbranch_scc1 .Lmy_pf_fin
	s_waitcnt vmcnt(8)
	v_lshlrev_b32_e32 v7, 10, v7
	v_and_b32_e32 v7, 0xfffff000, v7
	v_lshlrev_b32_e32 v6, 10, v6
	v_and_b32_e32 v6, 0xfffff000, v6
	v_lshlrev_b32_e32 v9, 10, v9
	v_and_b32_e32 v9, 0xfffff000, v9
	v_lshlrev_b32_e32 v8, 10, v8
	v_and_b32_e32 v8, 0xfffff000, v8
.Lmy_pf_fin:
	v_lshlrev_b32_e32 v17, 4, v3
	v_lshlrev_b32_e32 v15, 6, v11
	v_and_b32_e32 v16, 32, v3
	v_and_b32_e32 v17, 48, v17
	v_bitop3_b32 v15, v17, v15, v16 bitop3:0xde
	v_or_b32_e32 v221, v9, v15
	v_lshlrev_b32_e32 v9, 2, v12
	v_lshlrev_b32_e32 v11, 1, v11
	v_or3_b32 v9, v9, v11, v14
	v_lshlrev_b32_e32 v11, 2, v3
	v_and_b32_e32 v12, 0xfffffc00, v11
	v_lshl_add_u32 v9, v9, 11, v12
	v_lshlrev_b32_e32 v12, 8, v13
	v_lshlrev_b32_e32 v10, 4, v10
	v_and_or_b32 v10, v10, 48, v12
	v_lshlrev_b32_e32 v12, 3, v3
	v_or_b32_e32 v223, v7, v15
	v_and_b32_e32 v7, 15, v3
	v_and_b32_e32 v12, 32, v12
	v_or_b32_e32 v222, v6, v15
	v_ashrrev_i32_e32 v6, 8, v3
	v_bitop3_b32 v219, v9, v10, v12 bitop3:0xf6
	v_lshlrev_b32_e32 v7, 6, v7
	v_and_b32_e32 v3, 48, v3
	v_and_b32_e32 v10, 32, v11
	v_or_b32_e32 v9, v7, v3
	v_bitop3_b32 v3, v7, v10, v3 bitop3:0x36
	v_lshlrev_b32_e32 v11, 13, v5
	v_lshlrev_b32_e32 v220, 6, v14
	v_lshlrev_b32_e32 v4, 4, v4
	v_lshlrev_b32_e32 v7, 14, v6
	v_and_or_b32 v226, v11, s66, v3
	v_cmp_eq_u32_e32 vcc, 0, v215
	v_add_u32_e32 v227, 0, v219
	v_add_u32_e32 v3, 0xc0, v220
	v_or_b32_e32 v224, v8, v15
	v_lshl_or_b32 v229, v5, 10, v4
	v_bitop3_b32 v216, v9, v7, v10 bitop3:0xde
	v_or_b32_e32 v217, 0x8000, v226
	v_readfirstlane_b32 s1, v6
	s_and_b64 vcc, exec, vcc
	v_add_u32_e32 v228, v227, v220
	v_and_b32_e32 v218, 0xc0, v3
	v_readlane_b32 s7, v246, 3
	v_readlane_b32 s8, v246, 4
	v_readlane_b32 s9, v246, 5
	v_readlane_b32 s10, v246, 6
	v_readlane_b32 s11, v246, 7
	s_cbranch_vccnz .LBB0_1263
	s_sub_i32 s3, s87, s2
	s_mov_b32 s99, s3
	v_readfirstlane_b32 s100, v0
	s_nop 3
	s_lshr_b32 s100, s100, 7
	s_lshl_b32 s100, s100, 4
	s_add_i32 s3, s3, 15
	s_ashr_i32 s3, s3, 4
	s_cmp_eq_u32 s1, 0
	s_cselect_b32 s1, s3, 0
	v_readfirstlane_b32 s3, v229
	s_and_b32 s3, s3, 0xfffffc00
	s_add_i32 s3, s3, 0
	s_mov_b32 s38, s26
	s_mov_b32 s39, s27
	s_mov_b32 m0, s3
	s_waitcnt vmcnt(6)
	v_mov_b64_e32 v[4:5], v[118:119]
	s_cmp_lg_u32 s98, 0
	s_cbranch_scc0 .Lmy_pf_do0
	s_waitcnt vmcnt(0)
	s_branch .Lmy_pf_sk0
.Lmy_pf_do0:
	buffer_load_dwordx4 v223, s[36:39], 0 offen lds
.Lmy_pf_sk0:
	s_add_i32 m0, s3, 0x2000
	s_waitcnt vmcnt(3)
	v_mov_b64_e32 v[8:9], v[134:135]
	s_cmp_lg_u32 s98, 0
	s_cbranch_scc0 .Lmy_pf_do1
	s_waitcnt vmcnt(0)
	s_branch .Lmy_pf_sk1
.Lmy_pf_do1:
	buffer_load_dwordx4 v222, s[36:39], 0 offen lds
.Lmy_pf_sk1:
	s_add_i32 m0, s3, 0x4000
	v_mov_b64_e32 v[12:13], v[114:115]
	s_cmp_lg_u32 s98, 0
	s_cbranch_scc0 .Lmy_pf_do2
	s_waitcnt vmcnt(0)
	s_branch .Lmy_pf_sk2
.Lmy_pf_do2:
	buffer_load_dwordx4 v221, s[36:39], 0 offen lds
.Lmy_pf_sk2:
	s_add_i32 m0, s3, 0x6000
	s_waitcnt vmcnt(3)
	v_mov_b64_e32 v[16:17], v[146:147]
	v_mov_b64_e32 v[20:21], v[130:131]
	v_mov_b64_e32 v[24:25], v[122:123]
	v_mov_b64_e32 v[28:29], v[142:143]
	v_mov_b64_e32 v[32:33], v[126:127]
	s_cmp_lg_u32 s98, 0
	s_cbranch_scc0 .Lmy_pf_do3
	s_waitcnt vmcnt(0)
	s_branch .Lmy_pf_sk3
.Lmy_pf_do3:
	buffer_load_dwordx4 v224, s[36:39], 0 offen lds
.Lmy_pf_sk3:
	v_mov_b64_e32 v[6:7], v[120:121]
	v_mov_b64_e32 v[10:11], v[136:137]
	v_mov_b64_e32 v[14:15], v[116:117]
	v_mov_b64_e32 v[18:19], v[148:149]
	v_mov_b64_e32 v[22:23], v[132:133]
	v_mov_b64_e32 v[26:27], v[124:125]
	v_mov_b64_e32 v[30:31], v[144:145]
	v_mov_b64_e32 v[34:35], v[128:129]
	s_waitcnt vmcnt(0)
	s_movk_i32 s101, 0x80
	s_cmp_le_i32 s99, s100
	s_cbranch_scc1 .Lmy_rcgP0
	buffer_load_dwordx4 v[236:239], v223, s[36:39], s101 offen

; #define G_DMA_A(buf, t, i_) __builtin_amdgcn_raw_ptr_buffer_load_lds(ra, (LAS void*)(lds + (buf) * 65536 + a_wu + (i_) * 8192), 16, ao##i_, (unsigned)(t) * 128u, 0, 0)
; #define G_ISSUE_B(t) do { const unsigned so_ = (unsigned)(t) * 64u * ldbB; _Pragma("unroll") for (int i_ = 0; i_ < 8; ++i_) sb[i_] = __builtin_bit_cast(f32x4, __builtin_amdgcn_raw_buffer_load_b128(rb, bo, so_ + (unsigned)i_ * ldbB, 0)); } while (0)
; #define G_RETIRE() asm volatile("s_waitcnt vmcnt(0)" : "+v"(sb[0]), "+v"(sb[1]), "+v"(sb[2]), "+v"(sb[3]), "+v"(sb[4]), "+v"(sb[5]), "+v"(sb[6]), "+v"(sb[7]) :: "memory")
; #define G_WRITE_B(buf) do { LAS unsigned char* d_ = lds + (buf) * 65536; \
;         _Pragma("unroll") for (int j_ = 0; j_ < 4; ++j_) { u32x4 w_; w_.x = cvtpk(sb[0][j_], sb[1][j_]); w_.y = cvtpk(sb[2][j_], sb[3][j_]); w_.z = cvtpk(sb[4][j_], sb[5][j_]); w_.w = cvtpk(sb[6][j_], sb[7][j_]); \
;             *(LAS u32x4*)(d_ + 32768 + T.b_w + ((T.b_rot + 64u * j_) & 255u)) = w_; } } while (0)
; #define G_BAR() do { asm volatile("s_waitcnt lgkmcnt(0)" ::: "memory"); __builtin_amdgcn_s_barrier(); asm volatile("" ::: "memory"); } while (0)
; #define G_DMA_A(buf, t, i_) __builtin_amdgcn_raw_ptr_buffer_load_lds(ra, (LAS void*)(lds + (buf) * 65536 + a_wu + (i_) * 8192), 16, ao##i_, (unsigned)(t) * 128u, 0, 0)
; #define G_ISSUE_B(t) do { const unsigned so_ = (unsigned)(t) * 64u * ldbB; _Pragma("unroll") for (int i_ = 0; i_ < 8; ++i_) sb[i_] = __builtin_bit_cast(f32x4, __builtin_amdgcn_raw_buffer_load_b128(rb, bo, so_ + (unsigned)i_ * ldbB, 0)); } while (0)
; #define G_RETIRE() asm volatile("s_waitcnt vmcnt(0)" : "+v"(sb[0]), "+v"(sb[1]), "+v"(sb[2]), "+v"(sb[3]), "+v"(sb[4]), "+v"(sb[5]), "+v"(sb[6]), "+v"(sb[7]) :: "memory")
; __device__ __forceinline__ void gemm_kloop(f32x4 (&acc)[8][4], LAS unsigned char* lds, const GemmT& T, ...
;     ...
;     G_ISSUE_B(0); G_DMA_A(0, 0, 0); G_DMA_A(0, 0, 1); G_DMA_A(0, 0, 2); G_DMA_A(0, 0, 3); G_RETIRE(); G_WRITE_B(0);
;     if (nt > 1) G_ISSUE_B(1);
;     G_BAR();
; __device__ __forceinline__ void acc_zero(f32x4 (&acc)[8][4]) {
; #pragma unroll
;     for (int m = 0; m < 8; ++m)
; #pragma unroll
;         for (int n = 0; n < 4; ++n) acc[m][n] = (f32x4){0.f, 0.f, 0.f, 0.f};
.LBB0_1263:
	s_cbranch_execz .LBB0_1267
	v_readfirstlane_b32 s1, v229
	s_and_b32 s1, s1, 0xfffffc00
	s_add_i32 s1, s1, 0
	s_mov_b32 s38, s26
	s_mov_b32 s39, s27
	s_mov_b32 m0, s1
	v_add_u32_e32 v3, v227, v218
	s_cmp_lg_u32 s98, 0
	s_cbranch_scc1 .Lmy_pf_sk4
	buffer_load_dwordx4 v223, s[36:39], 0 offen lds
.Lmy_pf_sk4:
	s_add_i32 m0, s1, 0x2000
	v_mov_b32_e32 v36, 0
	s_cmp_lg_u32 s98, 0
	s_cbranch_scc1 .Lmy_pf_sk5
	buffer_load_dwordx4 v222, s[36:39], 0 offen lds
.Lmy_pf_sk5:
	s_add_i32 m0, s1, 0x4000
	s_mov_b32 s3, 0
	s_cmp_lg_u32 s98, 0
	s_cbranch_scc1 .Lmy_pf_sk6
	buffer_load_dwordx4 v221, s[36:39], 0 offen lds
.Lmy_pf_sk6:
	s_add_i32 m0, s1, 0x6000
	s_mov_b32 s4, 0x10e000
	s_cmp_lg_u32 s98, 0
	s_cbranch_scc1 .Lmy_pf_sk7
	buffer_load_dwordx4 v224, s[36:39], 0 offen lds
.Lmy_pf_sk7:
	s_waitcnt vmcnt(4)
	s_waitcnt vmcnt(0)
	s_movk_i32 s5, 0x80
	v_cvt_pk_bf16_f32 v4, v114, v126
	v_cvt_pk_bf16_f32 v5, v130, v118
	v_cvt_pk_bf16_f32 v6, v122, v134
	v_cvt_pk_bf16_f32 v7, v142, v146
	ds_write_b128 v228, v[4:7] offset:32768
	v_cvt_pk_bf16_f32 v4, v115, v127
	v_cvt_pk_bf16_f32 v5, v131, v119
	v_cvt_pk_bf16_f32 v6, v123, v135
	v_cvt_pk_bf16_f32 v7, v143, v147
	ds_write_b128 v228, v[4:7] offset:32832
	v_cvt_pk_bf16_f32 v4, v116, v128
	v_cvt_pk_bf16_f32 v5, v132, v120
	v_cvt_pk_bf16_f32 v6, v124, v136
	v_cvt_pk_bf16_f32 v7, v144, v148
	ds_write_b128 v228, v[4:7] offset:32896
	v_cvt_pk_bf16_f32 v4, v117, v129
	v_cvt_pk_bf16_f32 v5, v133, v121
	v_cvt_pk_bf16_f32 v6, v125, v137
	v_cvt_pk_bf16_f32 v7, v145, v149
	ds_write_b128 v3, v[4:7] offset:32768
	buffer_load_dwordx4 v[4:7], v225, s[24:27], s67 offen
	buffer_load_dwordx4 v[8:11], v225, s[24:27], s76 offen
	buffer_load_dwordx4 v[12:15], v225, s[24:27], s77 offen
	buffer_load_dwordx4 v[16:19], v225, s[24:27], s78 offen
	buffer_load_dwordx4 v[20:23], v225, s[24:27], s79 offen
	buffer_load_dwordx4 v[28:31], v225, s[24:27], s80 offen
	buffer_load_dwordx4 v[24:27], v225, s[24:27], s81 offen
	buffer_load_dwordx4 v[32:35], v225, s[24:27], s82 offen
	s_waitcnt lgkmcnt(0)
	s_barrier
	v_mov_b32_e32 v37, v36
	v_mov_b32_e32 v38, v36
	v_mov_b32_e32 v39, v36
	v_mov_b32_e32 v40, v36
	v_mov_b32_e32 v41, v36
	v_mov_b32_e32 v42, v36
	v_mov_b32_e32 v43, v36
	v_mov_b32_e32 v44, v36
	v_mov_b32_e32 v45, v36
	v_mov_b32_e32 v46, v36
	v_mov_b32_e32 v47, v36
	v_mov_b32_e32 v48, v36
	v_mov_b32_e32 v49, v36
	v_mov_b32_e32 v50, v36
	v_mov_b32_e32 v51, v36
	v_mov_b32_e32 v52, v36
	v_mov_b32_e32 v53, v36
	v_mov_b32_e32 v54, v36
	v_mov_b32_e32 v55, v36
	v_mov_b32_e32 v56, v36
	v_mov_b32_e32 v57, v36
	v_mov_b32_e32 v58, v36
	v_mov_b32_e32 v59, v36
	v_mov_b32_e32 v60, v36
	v_mov_b32_e32 v61, v36
	v_mov_b32_e32 v62, v36
	v_mov_b32_e32 v63, v36
	v_mov_b32_e32 v64, v36
	v_mov_b32_e32 v65, v36
	v_mov_b32_e32 v66, v36
	v_mov_b32_e32 v67, v36
	v_mov_b32_e32 v68, v36
	v_mov_b32_e32 v69, v36
	v_mov_b32_e32 v70, v36
	v_mov_b32_e32 v71, v36
	v_mov_b32_e32 v72, v36
	v_mov_b32_e32 v73, v36
	v_mov_b32_e32 v74, v36
	v_mov_b32_e32 v75, v36
	v_mov_b32_e32 v76, v36
	v_mov_b32_e32 v77, v36
	v_mov_b32_e32 v78, v36
	v_mov_b32_e32 v79, v36
	v_mov_b32_e32 v80, v36
	v_mov_b32_e32 v81, v36
	v_mov_b32_e32 v82, v36
	v_mov_b32_e32 v83, v36
	v_mov_b32_e32 v84, v36
	v_mov_b32_e32 v85, v36
	v_mov_b32_e32 v86, v36
	v_mov_b32_e32 v87, v36
	v_mov_b32_e32 v88, v36
	v_mov_b32_e32 v89, v36
	v_mov_b32_e32 v90, v36
	v_mov_b32_e32 v91, v36
	v_mov_b32_e32 v92, v36
	v_mov_b32_e32 v93, v36
	v_mov_b32_e32 v94, v36
	v_mov_b32_e32 v95, v36
	v_mov_b32_e32 v96, v36
	v_mov_b32_e32 v97, v36
	v_mov_b32_e32 v98, v36
	v_mov_b32_e32 v99, v36
	v_mov_b32_e32 v100, v36
	v_mov_b32_e32 v101, v36
	v_mov_b32_e32 v102, v36
	v_mov_b32_e32 v103, v36
	v_mov_b32_e32 v104, v36
	v_mov_b32_e32 v105, v36
	v_mov_b32_e32 v106, v36
	v_mov_b32_e32 v107, v36
	v_mov_b32_e32 v108, v36
	v_mov_b32_e32 v109, v36
	v_mov_b32_e32 v110, v36
	v_mov_b32_e32 v111, v36
	v_mov_b32_e32 v112, v36
	v_mov_b32_e32 v113, v36
	v_mov_b32_e32 v114, v36
	v_mov_b32_e32 v115, v36
	v_mov_b32_e32 v116, v36
	v_mov_b32_e32 v117, v36
	v_mov_b32_e32 v118, v36
	v_mov_b32_e32 v119, v36
	v_mov_b32_e32 v120, v36
	v_mov_b32_e32 v121, v36
	v_mov_b32_e32 v122, v36
	v_mov_b32_e32 v123, v36
	v_mov_b32_e32 v124, v36
	v_mov_b32_e32 v125, v36
	v_mov_b32_e32 v126, v36
	v_mov_b32_e32 v127, v36
	v_mov_b32_e32 v128, v36
	v_mov_b32_e32 v129, v36
	v_mov_b32_e32 v130, v36
	v_mov_b32_e32 v131, v36
	v_mov_b32_e32 v132, v36
	v_mov_b32_e32 v133, v36
	v_mov_b32_e32 v134, v36
	v_mov_b32_e32 v135, v36
	v_mov_b32_e32 v136, v36
	v_mov_b32_e32 v137, v36
	v_mov_b32_e32 v138, v36
	v_mov_b32_e32 v139, v36
	v_mov_b32_e32 v140, v36
	v_mov_b32_e32 v141, v36
	v_mov_b32_e32 v142, v36
	v_mov_b32_e32 v143, v36
	v_mov_b32_e32 v144, v36
	v_mov_b32_e32 v145, v36
	v_mov_b32_e32 v146, v36
	v_mov_b32_e32 v147, v36
	v_mov_b32_e32 v148, v36
	v_mov_b32_e32 v149, v36
	v_mov_b32_e32 v150, v36
	v_mov_b32_e32 v151, v36
	v_mov_b32_e32 v152, v36
	v_mov_b32_e32 v153, v36
	v_mov_b32_e32 v154, v36
	v_mov_b32_e32 v155, v36
	v_mov_b32_e32 v156, v36
	v_mov_b32_e32 v157, v36
	v_mov_b32_e32 v158, v36
	v_mov_b32_e32 v159, v36
	v_mov_b32_e32 v160, v36
	v_mov_b32_e32 v161, v36
	v_mov_b32_e32 v162, v36
	v_mov_b32_e32 v163, v36

; __device__ __forceinline__ bool moe_unit(int cv, int u, int ntiles_n, MoeUnit& mu) {
;     int base = 0;
; #pragma unroll
;     for (int e = 0; e < E; ++e) { const int c = __builtin_amdgcn_readlane(cv, e), tm = (c + 255) >> 8, nu = tm * ntiles_n;
;         if (u < nu) { mu.e = e; mu.cnt = c; mu.base = base; mu.nt = u / tm; mu.mt = u - mu.nt * tm; mu.light = (mu.mt == tm - 1 && c - mu.mt * 256 <= 128) ? 1 : 0; return true; }
;         u -= nu; base += tm * 256; }
;     return false;
; }
; __device__ __forceinline__ void phase_moe_gu(const Ptrs& p, LAS unsigned char* lds) {
;     ...
;         const int* list = (const int*)(p.ws + OFF_LIST) + (size_t)mu.e * NTOK; const int i0 = mu.mt * 256, n0 = mu.nt * 128;
;         unsigned ao[4];
; #pragma unroll
;         for (int i = 0; i < 4; ++i) { const int r = i0 + T.aR + 64 * i; const int tok = (r < mu.cnt) ? (list[r] >> 2) : 0; ao[i] = (unsigned)((tok * D + T.aC) * 2); }
;         const float* wsel = ((__builtin_amdgcn_readfirstlane(T.b_p) & 1) ? p.w_up : p.w_gate) + (size_t)mu.e * D * D + n0;
.LBB0_1267:
	v_mov_b32_e32 v3, v0
	s_nop 0
	v_lshrrev_b32_e32 v4, 1, v3
	v_and_b32_e32 v4, 0x78, v4
	s_waitcnt vmcnt(3)
	s_add_i32 s98, s65, s33
	s_mov_b32 s99, 0
.Lmy_pf_w:
	s_nop 1
	v_readlane_b32 s100, v1, s99
	s_add_i32 s101, s100, 0xff
	s_ashr_i32 s101, s101, 8
	s_lshl_b32 vcc_lo, s101, 4
	s_cmp_lt_i32 s98, vcc_lo
	s_cbranch_scc1 .Lmy_pf_found
	s_sub_i32 s98, s98, vcc_lo
	s_add_i32 s99, s99, 1
	s_cmp_lt_u32 s99, 32
	s_cbranch_scc1 .Lmy_pf_w
	s_mov_b32 s98, 0
	s_branch .Lmy_pf_none
.Lmy_pf_found:
	s_cmp_lt_i32 s98, s101
	s_cbranch_scc1 .Lmy_pf_mt
	s_sub_i32 s98, s98, s101
	s_branch .Lmy_pf_found
.Lmy_pf_mt:
	s_lshl_b32 vcc_lo, s99, 15
	s_add_u32 vcc_lo, s52, vcc_lo
	s_addc_u32 vcc_hi, s53, 0
	v_mov_b32_e32 v252, vcc_lo
	v_mov_b32_e32 v253, vcc_hi
	v_bfe_u32 v254, v0, 2, 4
	v_ashrrev_i32_e32 v251, 7, v0
	v_lshl_add_u32 v254, v251, 4, v254
	s_lshl_b32 s101, s98, 8
	v_or_b32_e32 v254, s101, v254
	v_mov_b32_e32 v255, 0
	v_lshl_add_u64 v[252:253], v[254:255], 2, v[252:253]
	v_mov_b32_e32 v247, 0
	v_mov_b32_e32 v248, 0
	v_mov_b32_e32 v249, 0
	v_mov_b32_e32 v250, 0
	v_cmp_gt_i32_e32 vcc, s100, v254
	s_and_saveexec_b64 s[98:99], vcc
	global_load_dword v247, v[252:253], off
	s_or_b64 exec, exec, s[98:99]
	v_add_u32_e32 v251, 64, v254
	v_cmp_gt_i32_e32 vcc, s100, v251
	s_and_saveexec_b64 s[98:99], vcc
	global_load_dword v248, v[252:253], off offset:256
	s_or_b64 exec, exec, s[98:99]
	v_add_u32_e32 v251, 128, v254
	v_cmp_gt_i32_e32 vcc, s100, v251
	s_and_saveexec_b64 s[98:99], vcc
	global_load_dword v249, v[252:253], off offset:512
	s_or_b64 exec, exec, s[98:99]
	v_add_u32_e32 v251, 192, v254
	v_cmp_gt_i32_e32 vcc, s100, v251
	s_and_saveexec_b64 s[98:99], vcc
	global_load_dword v250, v[252:253], off offset:768
	s_or_b64 exec, exec, s[98:99]
	s_mov_b32 s98, 1
.Lmy_pf_none:
	v_or_b32_e32 v130, s0, v4
	s_lshl_b64 s[0:1], s[42:43], 13
	s_add_u32 s4, s50, s0
	v_ashrrev_i32_e32 v131, 31, v130
	s_addc_u32 s5, s51, s1
	v_lshlrev_b64 v[4:5], 2, v[130:131]
	v_lshl_add_u64 v[114:115], s[4:5], 0, v[4:5]
	v_readlane_b32 s4, v246, 0
	v_readlane_b32 s6, v246, 2
	v_readlane_b32 s7, v246, 3
	s_add_u32 s0, s6, s0
	s_addc_u32 s1, s7, s1
	v_lshl_add_u64 v[4:5], s[0:1], 0, v[4:5]
	global_load_dwordx4 v[126:129], v[114:115], off offset:16
	global_load_dwordx4 v[118:121], v[114:115], off
	s_nop 0
	global_load_dwordx4 v[114:117], v[4:5], off
	global_load_dwordx4 v[122:125], v[4:5], off offset:16
	v_ashrrev_i32_e32 v4, 1, v3
	v_and_b32_e32 v4, 0xffffff80, v4
	v_add_u32_e32 v4, s2, v4
	v_and_or_b32 v4, v3, 15, v4
	v_lshlrev_b32_e32 v3, 1, v130
	v_cmp_gt_i32_e32 vcc, s87, v4
	v_readlane_b32 s5, v246, 1
	v_readlane_b32 s8, v246, 4
	v_readlane_b32 s9, v246, 5
	v_readlane_b32 s10, v246, 6
	v_readlane_b32 s11, v246, 7
	s_waitcnt vmcnt(0)
	s_cmp_eq_u32 s98, 0
	s_cbranch_scc1 .Lmy_pf_nodma
	v_lshlrev_b32_e32 v247, 10, v247
	v_and_b32_e32 v247, 0xfffff000, v247
	v_lshlrev_b32_e32 v248, 10, v248
	v_and_b32_e32 v248, 0xfffff000, v248
	v_lshlrev_b32_e32 v249, 10, v249
	v_and_b32_e32 v249, 0xfffff000, v249
	v_lshlrev_b32_e32 v250, 10, v250
	v_and_b32_e32 v250, 0xfffff000, v250
	v_ashrrev_i32_e32 v251, 6, v0
	v_and_b32_e32 v251, 1, v251
	v_lshlrev_b32_e32 v252, 4, v0
	v_and_b32_e32 v252, 48, v252
	v_lshlrev_b32_e32 v251, 6, v251
	v_and_b32_e32 v253, 32, v0
	v_bitop3_b32 v251, v252, v251, v253 bitop3:0xde
	v_lshrrev_b32_e32 v252, 6, v0
	v_lshlrev_b32_e32 v252, 10, v252
	s_nop 1
	v_readfirstlane_b32 s100, v252
	s_mov_b32 s38, s26
	s_mov_b32 s39, s27
	v_or_b32_e32 v252, v247, v251
	s_mov_b32 m0, s100
	s_nop 0
	buffer_load_dwordx4 v252, s[36:39], 0 offen lds
	v_or_b32_e32 v253, v248, v251
	s_add_i32 m0, s100, 0x2000
	s_nop 0
	buffer_load_dwordx4 v253, s[36:39], 0 offen lds
	v_or_b32_e32 v254, v249, v251
	s_add_i32 m0, s100, 0x4000
	s_nop 0
	buffer_load_dwordx4 v254, s[36:39], 0 offen lds
	v_or_b32_e32 v255, v250, v251
	s_add_i32 m0, s100, 0x6000
	s_nop 0
	buffer_load_dwordx4 v255, s[36:39], 0 offen lds
; __device__ __forceinline__ float sigmoidf_(float x) { return __builtin_amdgcn_rcpf(1.0f + __builtin_amdgcn_exp2f(x * -1.4426950408889634f)); }
; __device__ __forceinline__ f32x4 rot1(const f32x4 a) { return (f32x4){a[1], a[2], a[3], a[0]}; }
; __device__ __forceinline__ u32x4 pack8(const f32x4 a, const f32x4 b) { u32x4 w; w.x = cvtpk(a[0], a[1]); w.y = cvtpk(a[2], a[3]); w.z = cvtpk(b[0], b[1]); w.w = cvtpk(b[2], b[3]); return w; }
; __device__ __forceinline__ void phase_moe_gu(const Ptrs& p, LAS unsigned char* lds) {
;     ...
; #pragma unroll
;         for (int m = 0; m < 8; ++m) { const int r = i0 + T.wr * 128 + m * 16 + T.fr;
;             f32x4 g0 = acc[m][0] + bg0, g1 = rot1(acc[m][1]) + bg1, u0 = acc[m][2] + bu0, u1 = rot1(acc[m][3]) + bu1;
; #pragma unroll
;             for (int j = 0; j < 4; ++j) { float g = fminf(g0[j], 7.0f), uu = fminf(fmaxf(u0[j], -7.0f), 7.0f); g0[j] = (uu + 1.0f) * g * sigmoidf_(1.702f * g);
;                 g = fminf(g1[j], 7.0f); uu = fminf(fmaxf(u1[j], -7.0f), 7.0f); g1[j] = (uu + 1.0f) * g * sigmoidf_(1.702f * g); }
;             if (r < mu.cnt) __builtin_amdgcn_raw_buffer_store_b128(pack8(g0, g1), ract, (unsigned)(((mu.base + r) * D + c) * 2), 0, 16); }
.Lmy_pf_nodma:
	s_and_saveexec_b64 s[0:1], vcc
	s_cbranch_execz .LBB0_1269
	v_pk_mov_b32 v[130:131], v[194:195], v[196:197] op_sel:[1,0]
	v_add_f32_e32 v5, v159, v122
	v_pk_add_f32 v[130:131], v[130:131], v[126:127]
	v_med3_f32 v134, v5, s84, v214
	v_min_f32_e32 v130, 0x40e00000, v130
	v_min_f32_e32 v131, 0x40e00000, v131
	v_mul_f32_e32 v5, 0x3fd9db23, v130
	v_mul_f32_e32 v135, 0x3fd9db23, v131
	v_mul_f32_e32 v5, 0xbfb8aa3b, v5
	v_mul_f32_e32 v135, 0xbfb8aa3b, v135
	v_exp_f32_e32 v5, v5
	v_exp_f32_e32 v135, v135
	v_pk_mov_b32 v[132:133], v[196:197], v[194:195] op_sel:[1,0]
	s_mov_b32 s22, s26
	v_add_f32_e32 v5, 1.0, v5
	v_add_f32_e32 v135, 1.0, v135
	v_rcp_f32_e32 v136, v5
	v_add_f32_e32 v5, v160, v123
	v_rcp_f32_e32 v137, v135
	v_med3_f32 v135, v5, s84, v214
	v_pk_add_f32 v[134:135], v[134:135], 1.0 op_sel_hi:[1,0]
	v_pk_add_f32 v[132:133], v[132:133], v[128:129]
	v_pk_mul_f32 v[130:131], v[130:131], v[134:135]
	v_add_f32_e32 v5, v161, v124
	v_pk_mul_f32 v[134:135], v[130:131], v[136:137]
	v_min_f32_e32 v130, 0x40e00000, v132
	v_med3_f32 v132, v5, s84, v214
	v_mul_f32_e32 v5, 0x3fd9db23, v130
	v_min_f32_e32 v131, 0x40e00000, v133
	v_mul_f32_e32 v5, 0xbfb8aa3b, v5
	v_mul_f32_e32 v133, 0x3fd9db23, v131
	v_exp_f32_e32 v5, v5
	v_mul_f32_e32 v133, 0xbfb8aa3b, v133
	v_exp_f32_e32 v133, v133
	s_mov_b32 s23, s27
	v_add_f32_e32 v5, 1.0, v5
	v_rcp_f32_e32 v136, v5
	v_add_f32_e32 v5, v158, v125
	v_add_f32_e32 v133, 1.0, v133
	v_rcp_f32_e32 v137, v133
	v_med3_f32 v133, v5, s84, v214
	v_pk_add_f32 v[132:133], v[132:133], 1.0 op_sel_hi:[1,0]
	v_add_f32_e32 v5, v150, v114
	v_pk_mul_f32 v[130:131], v[130:131], v[132:133]
	v_pk_add_f32 v[132:133], v[154:155], v[118:119]
	v_med3_f32 v142, v5, s84, v214
	v_min_f32_e32 v132, 0x40e00000, v132
	v_mul_f32_e32 v5, 0x3fd9db23, v132
	v_min_f32_e32 v133, 0x40e00000, v133
	v_mul_f32_e32 v5, 0xbfb8aa3b, v5
	v_mul_f32_e32 v143, 0x3fd9db23, v133
	v_exp_f32_e32 v5, v5
	v_mul_f32_e32 v143, 0xbfb8aa3b, v143
	v_exp_f32_e32 v143, v143
	v_pk_mul_f32 v[136:137], v[130:131], v[136:137]
	v_add_f32_e32 v5, 1.0, v5
	v_rcp_f32_e32 v144, v5
	v_add_f32_e32 v5, v151, v115
	v_add_f32_e32 v143, 1.0, v143
	v_pk_add_f32 v[130:131], v[156:157], v[120:121]
	v_rcp_f32_e32 v145, v143
	v_med3_f32 v143, v5, s84, v214
	v_pk_add_f32 v[142:143], v[142:143], 1.0 op_sel_hi:[1,0]
	v_min_f32_e32 v130, 0x40e00000, v130
	v_add_f32_e32 v5, v152, v116
	v_min_f32_e32 v131, 0x40e00000, v131
	v_pk_mul_f32 v[132:133], v[132:133], v[142:143]
	v_med3_f32 v142, v5, s84, v214
	v_mul_f32_e32 v5, 0x3fd9db23, v130
	v_mul_f32_e32 v143, 0x3fd9db23, v131
	v_mul_f32_e32 v5, 0xbfb8aa3b, v5
	v_mul_f32_e32 v143, 0xbfb8aa3b, v143
	v_exp_f32_e32 v5, v5
	v_exp_f32_e32 v143, v143
	v_pk_mul_f32 v[132:133], v[132:133], v[144:145]
	v_add_f32_e32 v5, 1.0, v5
	v_add_f32_e32 v143, 1.0, v143
	v_rcp_f32_e32 v144, v5
	v_add_f32_e32 v5, v153, v117
	v_rcp_f32_e32 v145, v143
	v_med3_f32 v143, v5, s84, v214
	v_pk_add_f32 v[142:143], v[142:143], 1.0 op_sel_hi:[1,0]
	v_add_u32_e32 v5, s88, v4
	v_pk_mul_f32 v[130:131], v[130:131], v[142:143]
	v_lshl_add_u32 v5, v5, 12, v3
	v_pk_mul_f32 v[142:143], v[130:131], v[144:145]
	v_cvt_pk_bf16_f32 v130, v132, v133
	v_cvt_pk_bf16_f32 v131, v142, v143
	v_cvt_pk_bf16_f32 v132, v134, v135
	v_cvt_pk_bf16_f32 v133, v136, v137
	buffer_store_dwordx4 v[130:133], v5, s[20:23], 0 offen sc1
